# combo6 = combo5 + router commit biases batched + MoE token-index slices fetched together
# baseline (speedup 1.0000x reference)
.LBB0_936:
	s_or_b64 exec, exec, s[8:9]
	s_lshl_b32 s78, s77, 6
	s_add_i32 s8, s78, s54
	s_ashr_i32 s9, s8, 31
	s_lshl_b64 s[10:11], s[8:9], 12
	s_add_u32 s10, s52, s10
	s_addc_u32 s11, s53, s11
	v_lshl_add_u64 v[16:17], s[10:11], 0, v[126:127]
	v_add_co_u32_e32 v2, vcc, s75, v16
	s_waitcnt lgkmcnt(0)
	s_barrier
	global_load_dwordx2 v[14:15], v126, s[10:11]
	v_addc_co_u32_e32 v3, vcc, 0, v17, vcc
	global_load_dwordx2 v[18:19], v[2:3], off
	global_load_dwordx4 v[10:13], v[128:129], off
	v_mov_b32_e32 v2, s55
	ds_read_b128 v[6:9], v2 offset:20736
	ds_read_b128 v[2:5], v2 offset:20752
	v_mov_b32_e32 v20, v127
	v_mov_b32_e32 v21, v127
	s_lshl_b64 s[8:9], s[8:9], 11
	v_lshl_add_u64 v[36:37], v[138:139], 0, s[8:9]
	v_lshl_add_u64 v[16:17], v[16:17], 0, s[42:43]
	global_load_dwordx2 v[22:23], v126, s[10:11] offset:512
	global_load_dwordx2 v[24:25], v126, s[10:11] offset:1024
	global_load_dwordx2 v[26:27], v126, s[10:11] offset:1536
	global_load_dwordx2 v[28:29], v126, s[10:11] offset:2048
	global_load_dwordx2 v[30:31], v126, s[10:11] offset:2560
	global_load_dwordx2 v[32:33], v126, s[10:11] offset:3072
	global_load_dwordx2 v[34:35], v126, s[10:11] offset:3584
	global_load_dwordx2 v[38:39], v[16:17], off offset:2560
	global_load_dwordx2 v[40:41], v[16:17], off offset:3072
	global_load_dwordx2 v[42:43], v[16:17], off offset:3584
	v_mov_b32_e32 v48, v127
	v_mov_b32_e32 v49, v127
	s_add_i32 s8, s78, s56
	s_ashr_i32 s9, s8, 31
	s_lshl_b64 s[10:11], s[8:9], 12
	s_add_u32 s10, s52, s10
	s_addc_u32 s11, s53, s11
	s_lshl_b64 s[8:9], s[8:9], 11
	s_waitcnt vmcnt(12)
	v_lshlrev_b32_e32 v44, 16, v14
	v_and_b32_e32 v45, 0xffff0000, v14
	s_waitcnt lgkmcnt(1)
	v_pk_mul_f32 v[44:45], v[6:7], v[44:45] op_sel_hi:[0,1]
	s_waitcnt vmcnt(11)
	v_lshlrev_b32_e32 v46, 16, v18
	v_and_b32_e32 v47, 0xffff0000, v18
	s_waitcnt vmcnt(10)
	v_pk_mul_f32 v[44:45], v[44:45], v[10:11]
	v_pk_mul_f32 v[46:47], v[6:7], v[46:47] op_sel:[1,0]
	v_cvt_pk_fp8_f32 v20, v44, v45
	v_pk_mul_f32 v[10:11], v[46:47], v[10:11]
	v_lshlrev_b32_e32 v14, 16, v15
	v_and_b32_e32 v15, 0xffff0000, v15
	v_cvt_pk_fp8_f32 v21, v10, v11
	v_pk_mul_f32 v[14:15], v[6:7], v[14:15] op_sel_hi:[0,1]
	v_lshlrev_b32_e32 v18, 16, v19
	v_and_b32_e32 v19, 0xffff0000, v19
	v_pk_mul_f32 v[14:15], v[14:15], v[12:13]
	v_pk_mul_f32 v[10:11], v[6:7], v[18:19] op_sel:[1,0]
	v_cvt_pk_fp8_f32 v20, v14, v15 op_sel:[0,0,1]
	v_pk_mul_f32 v[10:11], v[10:11], v[12:13]
	global_load_dwordx2 v[14:15], v[16:17], off offset:512
	global_load_dwordx2 v[18:19], v[16:17], off offset:1024
	global_load_dwordx2 v[44:45], v[16:17], off offset:1536
	s_nop 0
	global_load_dwordx2 v[16:17], v[16:17], off offset:2048
	v_cvt_pk_fp8_f32 v21, v10, v11 op_sel:[0,0,1]
	global_store_dword v[36:37], v20, off
	global_store_dword v[36:37], v21, off offset:2048
	global_load_dwordx4 v[10:13], v[128:129], off offset:1024
	s_waitcnt vmcnt(16)
	v_lshlrev_b32_e32 v20, 16, v22
	v_and_b32_e32 v21, 0xffff0000, v22
	v_pk_mul_f32 v[20:21], v[6:7], v[20:21] op_sel_hi:[0,1]
	v_lshlrev_b32_e32 v22, 16, v23
	v_and_b32_e32 v23, 0xffff0000, v23
	v_pk_mul_f32 v[22:23], v[6:7], v[22:23] op_sel_hi:[0,1]
	s_waitcnt vmcnt(6)
	v_lshlrev_b32_e32 v46, 16, v14
	v_and_b32_e32 v47, 0xffff0000, v14
	v_pk_mul_f32 v[46:47], v[6:7], v[46:47] op_sel:[1,0]
	v_lshlrev_b32_e32 v14, 16, v15
	v_and_b32_e32 v15, 0xffff0000, v15
	v_pk_mul_f32 v[14:15], v[6:7], v[14:15] op_sel:[1,0]
	s_waitcnt vmcnt(0)
	v_pk_mul_f32 v[20:21], v[20:21], v[10:11]
	v_pk_mul_f32 v[10:11], v[46:47], v[10:11]
	v_cvt_pk_fp8_f32 v48, v20, v21
	v_cvt_pk_fp8_f32 v49, v10, v11
	v_pk_mul_f32 v[10:11], v[22:23], v[12:13]
	v_pk_mul_f32 v[12:13], v[14:15], v[12:13]
	v_cvt_pk_fp8_f32 v48, v10, v11 op_sel:[0,0,1]
	v_cvt_pk_fp8_f32 v49, v12, v13 op_sel:[0,0,1]
	global_store_dword v[36:37], v48, off offset:256
	global_store_dword v[36:37], v49, off offset:2304
	global_load_dwordx4 v[10:13], v[128:129], off offset:2048
	v_lshlrev_b32_e32 v14, 16, v24
	v_and_b32_e32 v15, 0xffff0000, v24
	v_pk_mul_f32 v[14:15], v[6:7], v[14:15] op_sel_hi:[0,1]
	v_lshlrev_b32_e32 v22, 16, v18
	v_and_b32_e32 v23, 0xffff0000, v18
	v_mov_b32_e32 v46, v127
	v_pk_mul_f32 v[22:23], v[6:7], v[22:23] op_sel:[1,0]
	v_mov_b32_e32 v47, v127
	v_lshlrev_b32_e32 v20, 16, v25
	v_and_b32_e32 v21, 0xffff0000, v25
	v_pk_mul_f32 v[20:21], v[6:7], v[20:21] op_sel_hi:[0,1]
	v_lshlrev_b32_e32 v18, 16, v19
	v_and_b32_e32 v19, 0xffff0000, v19
	v_pk_mul_f32 v[18:19], v[6:7], v[18:19] op_sel:[1,0]
	v_mov_b32_e32 v24, v127
	v_mov_b32_e32 v25, v127
	s_waitcnt vmcnt(0)
	v_pk_mul_f32 v[14:15], v[14:15], v[10:11]
	v_pk_mul_f32 v[10:11], v[22:23], v[10:11]
	v_cvt_pk_fp8_f32 v46, v14, v15
	v_cvt_pk_fp8_f32 v47, v10, v11
	v_pk_mul_f32 v[10:11], v[20:21], v[12:13]
	v_pk_mul_f32 v[12:13], v[18:19], v[12:13]
	v_cvt_pk_fp8_f32 v46, v10, v11 op_sel:[0,0,1]
	v_cvt_pk_fp8_f32 v47, v12, v13 op_sel:[0,0,1]
	global_store_dword v[36:37], v46, off offset:512
	global_store_dword v[36:37], v47, off offset:2560
	global_load_dwordx4 v[10:13], v[128:129], off offset:3072
	v_lshlrev_b32_e32 v14, 16, v26
	v_and_b32_e32 v15, 0xffff0000, v26
	v_pk_mul_f32 v[14:15], v[6:7], v[14:15] op_sel_hi:[0,1]
	v_lshlrev_b32_e32 v20, 16, v44
	v_and_b32_e32 v21, 0xffff0000, v44
	v_pk_mul_f32 v[20:21], v[6:7], v[20:21] op_sel:[1,0]
	v_lshlrev_b32_e32 v18, 16, v27
	v_and_b32_e32 v19, 0xffff0000, v27
	v_pk_mul_f32 v[18:19], v[6:7], v[18:19] op_sel_hi:[0,1]
	v_lshlrev_b32_e32 v22, 16, v45
	v_and_b32_e32 v23, 0xffff0000, v45
	v_pk_mul_f32 v[22:23], v[6:7], v[22:23] op_sel:[1,0]
	v_mov_b32_e32 v44, v127
	s_waitcnt vmcnt(0)
	v_pk_mul_f32 v[14:15], v[14:15], v[10:11]
	v_pk_mul_f32 v[10:11], v[20:21], v[10:11]
	v_cvt_pk_fp8_f32 v24, v14, v15
	v_cvt_pk_fp8_f32 v25, v10, v11
	v_pk_mul_f32 v[10:11], v[18:19], v[12:13]
	v_pk_mul_f32 v[12:13], v[22:23], v[12:13]
	v_cvt_pk_fp8_f32 v24, v10, v11 op_sel:[0,0,1]
	v_cvt_pk_fp8_f32 v25, v12, v13 op_sel:[0,0,1]
	global_store_dword v[36:37], v24, off offset:768
	global_store_dword v[36:37], v25, off offset:2816
	global_load_dwordx4 v[10:13], v[130:131], off
	v_lshlrev_b32_e32 v14, 16, v28
	v_and_b32_e32 v15, 0xffff0000, v28
	v_pk_mul_f32 v[14:15], v[6:7], v[14:15] op_sel_hi:[0,1]
	v_lshlrev_b32_e32 v20, 16, v16
	v_and_b32_e32 v21, 0xffff0000, v16
	v_mov_b32_e32 v22, v127
	v_pk_mul_f32 v[20:21], v[6:7], v[20:21] op_sel:[1,0]
	v_mov_b32_e32 v23, v127
	v_lshlrev_b32_e32 v18, 16, v29
	v_and_b32_e32 v19, 0xffff0000, v29
	v_pk_mul_f32 v[18:19], v[6:7], v[18:19] op_sel_hi:[0,1]
	v_lshlrev_b32_e32 v16, 16, v17
	v_and_b32_e32 v17, 0xffff0000, v17
	v_pk_mul_f32 v[16:17], v[6:7], v[16:17] op_sel:[1,0]
	s_waitcnt vmcnt(0)
	v_pk_mul_f32 v[14:15], v[14:15], v[10:11]
	v_pk_mul_f32 v[10:11], v[20:21], v[10:11]
	v_cvt_pk_fp8_f32 v22, v14, v15
	v_cvt_pk_fp8_f32 v23, v10, v11
	v_pk_mul_f32 v[10:11], v[18:19], v[12:13]
	v_pk_mul_f32 v[12:13], v[16:17], v[12:13]
	v_cvt_pk_fp8_f32 v22, v10, v11 op_sel:[0,0,1]
	v_cvt_pk_fp8_f32 v23, v12, v13 op_sel:[0,0,1]
	global_store_dword v[36:37], v22, off offset:1024
	global_store_dword v[36:37], v23, off offset:3072
	global_load_dwordx4 v[10:13], v[132:133], off
	v_lshlrev_b32_e32 v14, 16, v30
	v_and_b32_e32 v15, 0xffff0000, v30
	v_pk_mul_f32 v[14:15], v[6:7], v[14:15] op_sel_hi:[0,1]
	v_lshlrev_b32_e32 v18, 16, v38
	v_and_b32_e32 v19, 0xffff0000, v38
	v_mov_b32_e32 v22, v127
	v_pk_mul_f32 v[18:19], v[6:7], v[18:19] op_sel:[1,0]
	v_mov_b32_e32 v23, v127
	v_lshlrev_b32_e32 v16, 16, v31
	v_and_b32_e32 v17, 0xffff0000, v31
	v_pk_mul_f32 v[16:17], v[6:7], v[16:17] op_sel_hi:[0,1]
	v_lshlrev_b32_e32 v20, 16, v39
	v_and_b32_e32 v21, 0xffff0000, v39
	v_pk_mul_f32 v[20:21], v[6:7], v[20:21] op_sel:[1,0]
	s_waitcnt vmcnt(0)
	v_pk_mul_f32 v[14:15], v[14:15], v[10:11]
	v_pk_mul_f32 v[10:11], v[18:19], v[10:11]
	v_cvt_pk_fp8_f32 v22, v14, v15
	v_cvt_pk_fp8_f32 v23, v10, v11
	v_pk_mul_f32 v[10:11], v[16:17], v[12:13]
	v_pk_mul_f32 v[12:13], v[20:21], v[12:13]
	v_cvt_pk_fp8_f32 v22, v10, v11 op_sel:[0,0,1]
	v_cvt_pk_fp8_f32 v23, v12, v13 op_sel:[0,0,1]
	global_store_dword v[36:37], v22, off offset:1280
	global_store_dword v[36:37], v23, off offset:3328
	global_load_dwordx4 v[10:13], v[134:135], off
	v_lshlrev_b32_e32 v14, 16, v32
	v_and_b32_e32 v15, 0xffff0000, v32
	v_pk_mul_f32 v[14:15], v[6:7], v[14:15] op_sel_hi:[0,1]
	v_lshlrev_b32_e32 v18, 16, v40
	v_and_b32_e32 v19, 0xffff0000, v40
	v_mov_b32_e32 v22, v127
	v_pk_mul_f32 v[18:19], v[6:7], v[18:19] op_sel:[1,0]
	v_mov_b32_e32 v23, v127
	v_lshlrev_b32_e32 v16, 16, v33
	v_and_b32_e32 v17, 0xffff0000, v33
	v_pk_mul_f32 v[16:17], v[6:7], v[16:17] op_sel_hi:[0,1]
	v_lshlrev_b32_e32 v20, 16, v41
	v_and_b32_e32 v21, 0xffff0000, v41
	v_pk_mul_f32 v[20:21], v[6:7], v[20:21] op_sel:[1,0]
	s_waitcnt vmcnt(0)
	v_pk_mul_f32 v[14:15], v[14:15], v[10:11]
	v_pk_mul_f32 v[10:11], v[18:19], v[10:11]
	v_cvt_pk_fp8_f32 v22, v14, v15
	v_cvt_pk_fp8_f32 v23, v10, v11
	v_pk_mul_f32 v[10:11], v[16:17], v[12:13]
	v_pk_mul_f32 v[12:13], v[20:21], v[12:13]
	v_cvt_pk_fp8_f32 v22, v10, v11 op_sel:[0,0,1]
	v_cvt_pk_fp8_f32 v23, v12, v13 op_sel:[0,0,1]
	global_store_dword v[36:37], v22, off offset:1536
	global_store_dword v[36:37], v23, off offset:3584
	global_load_dwordx4 v[10:13], v[136:137], off
	v_lshlrev_b32_e32 v14, 16, v34
	v_and_b32_e32 v15, 0xffff0000, v34
	v_pk_mul_f32 v[14:15], v[6:7], v[14:15] op_sel_hi:[0,1]
	v_lshlrev_b32_e32 v18, 16, v42
	v_and_b32_e32 v19, 0xffff0000, v42
	v_mov_b32_e32 v22, v127
	v_pk_mul_f32 v[18:19], v[6:7], v[18:19] op_sel:[1,0]
	v_mov_b32_e32 v23, v127
	v_lshlrev_b32_e32 v16, 16, v35
	v_and_b32_e32 v17, 0xffff0000, v35
	v_pk_mul_f32 v[16:17], v[6:7], v[16:17] op_sel_hi:[0,1]
	v_lshlrev_b32_e32 v20, 16, v43
	v_and_b32_e32 v21, 0xffff0000, v43
	v_pk_mul_f32 v[6:7], v[6:7], v[20:21] op_sel:[1,0]
	v_lshl_add_u64 v[20:21], v[138:139], 0, s[8:9]
	s_waitcnt vmcnt(0)
	v_pk_mul_f32 v[14:15], v[14:15], v[10:11]
	v_pk_mul_f32 v[10:11], v[18:19], v[10:11]
	v_cvt_pk_fp8_f32 v22, v14, v15
	v_cvt_pk_fp8_f32 v23, v10, v11
	v_pk_mul_f32 v[10:11], v[16:17], v[12:13]
	v_pk_mul_f32 v[6:7], v[6:7], v[12:13]
	v_cvt_pk_fp8_f32 v22, v10, v11 op_sel:[0,0,1]
	v_cvt_pk_fp8_f32 v23, v6, v7 op_sel:[0,0,1]
	v_lshl_add_u64 v[6:7], s[10:11], 0, v[126:127]
	global_store_dword v[36:37], v22, off offset:1792
	global_store_dword v[36:37], v23, off offset:3840
	global_load_dwordx2 v[14:15], v126, s[10:11]
	v_add_co_u32_e32 v10, vcc, s75, v6
	v_mov_b32_e32 v19, v127
	s_nop 0
	v_addc_co_u32_e32 v11, vcc, 0, v7, vcc
	global_load_dwordx2 v[16:17], v[10:11], off
	s_nop 0
	global_load_dwordx4 v[10:13], v[128:129], off
	v_mov_b32_e32 v18, v9
	v_lshl_add_u64 v[6:7], v[6:7], 0, s[42:43]
	global_load_dwordx2 v[22:23], v126, s[10:11] offset:512
	global_load_dwordx2 v[24:25], v126, s[10:11] offset:1024
	global_load_dwordx2 v[26:27], v126, s[10:11] offset:1536
	global_load_dwordx2 v[28:29], v[6:7], off offset:512
	global_load_dwordx2 v[30:31], v[6:7], off offset:1024
	global_load_dwordx2 v[32:33], v[6:7], off offset:1536
	global_load_dwordx2 v[34:35], v[6:7], off offset:2048
	global_load_dwordx2 v[36:37], v[6:7], off offset:2560
	global_load_dwordx2 v[38:39], v[6:7], off offset:3072
	s_nop 0
	global_load_dwordx2 v[6:7], v[6:7], off offset:3584
	s_waitcnt vmcnt(9)
	v_and_b32_e32 v45, 0xffff0000, v22
	v_lshlrev_b32_e32 v40, 16, v14
	v_and_b32_e32 v41, 0xffff0000, v14
	v_pk_mul_f32 v[40:41], v[8:9], v[40:41] op_sel_hi:[0,1]
	v_lshlrev_b32_e32 v14, 16, v15
	v_lshlrev_b32_e32 v42, 16, v16
	v_and_b32_e32 v43, 0xffff0000, v16
	v_lshlrev_b32_e32 v16, 16, v17
	v_and_b32_e32 v17, 0xffff0000, v17
	v_pk_mul_f32 v[42:43], v[18:19], v[42:43] op_sel_hi:[0,1]
	v_pk_mul_f32 v[40:41], v[40:41], v[10:11]
	v_pk_mul_f32 v[16:17], v[18:19], v[16:17] op_sel_hi:[0,1]
	v_pk_mul_f32 v[10:11], v[42:43], v[10:11]
	v_cvt_pk_fp8_f32 v19, v40, v41
	v_and_b32_e32 v15, 0xffff0000, v15
	v_cvt_pk_fp8_f32 v44, v10, v11
	v_pk_mul_f32 v[14:15], v[8:9], v[14:15] op_sel_hi:[0,1]
	v_pk_mul_f32 v[10:11], v[14:15], v[12:13]
	v_pk_mul_f32 v[12:13], v[16:17], v[12:13]
	v_cvt_pk_fp8_f32 v19, v10, v11 op_sel:[0,0,1]
	v_cvt_pk_fp8_f32 v44, v12, v13 op_sel:[0,0,1]
	global_load_dwordx2 v[14:15], v126, s[10:11] offset:2048
	global_load_dwordx2 v[16:17], v126, s[10:11] offset:2560
	global_load_dwordx2 v[40:41], v126, s[10:11] offset:3072
	global_load_dwordx2 v[42:43], v126, s[10:11] offset:3584
	s_nop 0
	global_store_dword v[20:21], v19, off
	global_store_dword v[20:21], v44, off offset:2048
	global_load_dwordx4 v[10:13], v[128:129], off offset:1024
	v_mov_b32_e32 v9, v127
	v_lshlrev_b32_e32 v44, 16, v22
	v_mov_b32_e32 v19, v127
	s_waitcnt vmcnt(13)
	v_lshlrev_b32_e32 v46, 16, v28
	v_and_b32_e32 v47, 0xffff0000, v28
	v_pk_mul_f32 v[44:45], v[8:9], v[44:45] op_sel_hi:[0,1]
	v_lshlrev_b32_e32 v22, 16, v23
	v_and_b32_e32 v23, 0xffff0000, v23
	v_pk_mul_f32 v[46:47], v[18:19], v[46:47] op_sel_hi:[0,1]
	v_lshlrev_b32_e32 v28, 16, v29
	v_and_b32_e32 v29, 0xffff0000, v29
	v_pk_mul_f32 v[22:23], v[8:9], v[22:23] op_sel_hi:[0,1]
	v_pk_mul_f32 v[28:29], v[18:19], v[28:29] op_sel_hi:[0,1]
	s_add_i32 s10, s78, s57
	s_ashr_i32 s11, s10, 31
	s_lshl_b64 s[8:9], s[10:11], 12
	s_add_u32 s8, s52, s8
	s_addc_u32 s9, s53, s9
	s_lshl_b64 s[10:11], s[10:11], 11
	s_waitcnt vmcnt(0)
	v_pk_mul_f32 v[44:45], v[44:45], v[10:11]
	v_pk_mul_f32 v[10:11], v[46:47], v[10:11]
	v_cvt_pk_fp8_f32 v9, v44, v45
	v_cvt_pk_fp8_f32 v19, v10, v11
	v_pk_mul_f32 v[10:11], v[22:23], v[12:13]
	v_pk_mul_f32 v[12:13], v[28:29], v[12:13]
	v_cvt_pk_fp8_f32 v9, v10, v11 op_sel:[0,0,1]
	v_cvt_pk_fp8_f32 v19, v12, v13 op_sel:[0,0,1]
	global_store_dword v[20:21], v9, off offset:256
	global_store_dword v[20:21], v19, off offset:2304
	global_load_dwordx4 v[10:13], v[128:129], off offset:2048
	v_mov_b32_e32 v9, v127
	v_lshlrev_b32_e32 v22, 16, v24
	v_and_b32_e32 v23, 0xffff0000, v24
	v_mov_b32_e32 v19, v127
	v_lshlrev_b32_e32 v28, 16, v30
	v_and_b32_e32 v29, 0xffff0000, v30
	v_pk_mul_f32 v[22:23], v[8:9], v[22:23] op_sel_hi:[0,1]
	v_lshlrev_b32_e32 v24, 16, v25
	v_and_b32_e32 v25, 0xffff0000, v25
	v_pk_mul_f32 v[28:29], v[18:19], v[28:29] op_sel_hi:[0,1]
	v_lshlrev_b32_e32 v30, 16, v31
	v_and_b32_e32 v31, 0xffff0000, v31
	v_pk_mul_f32 v[24:25], v[8:9], v[24:25] op_sel_hi:[0,1]
	v_pk_mul_f32 v[30:31], v[18:19], v[30:31] op_sel_hi:[0,1]
	v_mov_b32_e32 v44, v127
	v_mov_b32_e32 v45, v127
	s_waitcnt vmcnt(0)
	v_pk_mul_f32 v[22:23], v[22:23], v[10:11]
	v_pk_mul_f32 v[10:11], v[28:29], v[10:11]
	v_cvt_pk_fp8_f32 v9, v22, v23
	v_cvt_pk_fp8_f32 v19, v10, v11
	v_pk_mul_f32 v[10:11], v[24:25], v[12:13]
	v_pk_mul_f32 v[12:13], v[30:31], v[12:13]
	v_cvt_pk_fp8_f32 v9, v10, v11 op_sel:[0,0,1]
	v_cvt_pk_fp8_f32 v19, v12, v13 op_sel:[0,0,1]
	global_store_dword v[20:21], v9, off offset:512
	global_store_dword v[20:21], v19, off offset:2560
	global_load_dwordx4 v[10:13], v[128:129], off offset:3072
	v_mov_b32_e32 v9, v127
	v_lshlrev_b32_e32 v22, 16, v26
	v_and_b32_e32 v23, 0xffff0000, v26
	v_mov_b32_e32 v19, v127
	v_lshlrev_b32_e32 v24, 16, v27
	v_and_b32_e32 v25, 0xffff0000, v27
	v_lshlrev_b32_e32 v26, 16, v32
	v_and_b32_e32 v27, 0xffff0000, v32
	v_pk_mul_f32 v[22:23], v[8:9], v[22:23] op_sel_hi:[0,1]
	v_pk_mul_f32 v[26:27], v[18:19], v[26:27] op_sel_hi:[0,1]
	v_lshlrev_b32_e32 v28, 16, v33
	v_and_b32_e32 v29, 0xffff0000, v33
	v_pk_mul_f32 v[24:25], v[8:9], v[24:25] op_sel_hi:[0,1]
	v_pk_mul_f32 v[28:29], v[18:19], v[28:29] op_sel_hi:[0,1]
	s_waitcnt vmcnt(0)
	v_pk_mul_f32 v[22:23], v[22:23], v[10:11]
	v_pk_mul_f32 v[10:11], v[26:27], v[10:11]
	v_cvt_pk_fp8_f32 v9, v22, v23
	v_cvt_pk_fp8_f32 v19, v10, v11
	v_pk_mul_f32 v[10:11], v[24:25], v[12:13]
	v_pk_mul_f32 v[12:13], v[28:29], v[12:13]
	v_cvt_pk_fp8_f32 v9, v10, v11 op_sel:[0,0,1]
	v_cvt_pk_fp8_f32 v19, v12, v13 op_sel:[0,0,1]
	global_store_dword v[20:21], v9, off offset:768
	global_store_dword v[20:21], v19, off offset:2816
	global_load_dwordx4 v[10:13], v[130:131], off
	v_mov_b32_e32 v9, v127
	v_lshlrev_b32_e32 v22, 16, v14
	v_and_b32_e32 v23, 0xffff0000, v14
	v_mov_b32_e32 v19, v127
	v_lshlrev_b32_e32 v24, 16, v34
	v_and_b32_e32 v25, 0xffff0000, v34
	v_pk_mul_f32 v[22:23], v[8:9], v[22:23] op_sel_hi:[0,1]
	v_lshlrev_b32_e32 v14, 16, v15
	v_and_b32_e32 v15, 0xffff0000, v15
	v_pk_mul_f32 v[24:25], v[18:19], v[24:25] op_sel_hi:[0,1]
	v_lshlrev_b32_e32 v26, 16, v35
	v_and_b32_e32 v27, 0xffff0000, v35
	v_pk_mul_f32 v[14:15], v[8:9], v[14:15] op_sel_hi:[0,1]
	v_pk_mul_f32 v[26:27], v[18:19], v[26:27] op_sel_hi:[0,1]
	s_waitcnt vmcnt(0)
	v_pk_mul_f32 v[22:23], v[22:23], v[10:11]
	v_pk_mul_f32 v[10:11], v[24:25], v[10:11]
	v_cvt_pk_fp8_f32 v9, v22, v23
	v_cvt_pk_fp8_f32 v19, v10, v11
	v_pk_mul_f32 v[10:11], v[14:15], v[12:13]
	v_pk_mul_f32 v[12:13], v[26:27], v[12:13]
	v_cvt_pk_fp8_f32 v9, v10, v11 op_sel:[0,0,1]
	v_cvt_pk_fp8_f32 v19, v12, v13 op_sel:[0,0,1]
	global_store_dword v[20:21], v9, off offset:1024
	global_store_dword v[20:21], v19, off offset:3072
	global_load_dwordx4 v[10:13], v[132:133], off
	v_mov_b32_e32 v9, v127
	v_lshlrev_b32_e32 v14, 16, v16
	v_and_b32_e32 v15, 0xffff0000, v16
	v_mov_b32_e32 v19, v127
	v_lshlrev_b32_e32 v22, 16, v36
	v_and_b32_e32 v23, 0xffff0000, v36
	v_pk_mul_f32 v[14:15], v[8:9], v[14:15] op_sel_hi:[0,1]
	v_lshlrev_b32_e32 v16, 16, v17
	v_and_b32_e32 v17, 0xffff0000, v17
	v_pk_mul_f32 v[22:23], v[18:19], v[22:23] op_sel_hi:[0,1]
	v_lshlrev_b32_e32 v24, 16, v37
	v_and_b32_e32 v25, 0xffff0000, v37
	v_pk_mul_f32 v[16:17], v[8:9], v[16:17] op_sel_hi:[0,1]
	v_pk_mul_f32 v[24:25], v[18:19], v[24:25] op_sel_hi:[0,1]
	s_waitcnt vmcnt(0)
	v_pk_mul_f32 v[14:15], v[14:15], v[10:11]
	v_pk_mul_f32 v[10:11], v[22:23], v[10:11]
	v_cvt_pk_fp8_f32 v9, v14, v15
	v_cvt_pk_fp8_f32 v19, v10, v11
	v_pk_mul_f32 v[10:11], v[16:17], v[12:13]
	v_pk_mul_f32 v[12:13], v[24:25], v[12:13]
	v_cvt_pk_fp8_f32 v9, v10, v11 op_sel:[0,0,1]
	v_cvt_pk_fp8_f32 v19, v12, v13 op_sel:[0,0,1]
	global_store_dword v[20:21], v9, off offset:1280
	global_store_dword v[20:21], v19, off offset:3328
	global_load_dwordx4 v[10:13], v[134:135], off
	v_mov_b32_e32 v9, v127
	v_lshlrev_b32_e32 v14, 16, v40
	v_and_b32_e32 v15, 0xffff0000, v40
	v_mov_b32_e32 v19, v127
	v_lshlrev_b32_e32 v22, 16, v38
	v_and_b32_e32 v23, 0xffff0000, v38
	v_pk_mul_f32 v[14:15], v[8:9], v[14:15] op_sel_hi:[0,1]
	v_lshlrev_b32_e32 v16, 16, v41
	v_and_b32_e32 v17, 0xffff0000, v41
	v_pk_mul_f32 v[22:23], v[18:19], v[22:23] op_sel_hi:[0,1]
	v_lshlrev_b32_e32 v24, 16, v39
	v_and_b32_e32 v25, 0xffff0000, v39
	v_pk_mul_f32 v[16:17], v[8:9], v[16:17] op_sel_hi:[0,1]
	v_pk_mul_f32 v[24:25], v[18:19], v[24:25] op_sel_hi:[0,1]
	v_mov_b32_e32 v40, v127
	v_mov_b32_e32 v41, v127
	s_waitcnt vmcnt(0)
	v_pk_mul_f32 v[14:15], v[14:15], v[10:11]
	v_pk_mul_f32 v[10:11], v[22:23], v[10:11]
	v_cvt_pk_fp8_f32 v9, v14, v15
	v_cvt_pk_fp8_f32 v19, v10, v11
	v_pk_mul_f32 v[10:11], v[16:17], v[12:13]
	v_pk_mul_f32 v[12:13], v[24:25], v[12:13]
	v_cvt_pk_fp8_f32 v9, v10, v11 op_sel:[0,0,1]
	v_cvt_pk_fp8_f32 v19, v12, v13 op_sel:[0,0,1]
	global_store_dword v[20:21], v9, off offset:1536
	global_store_dword v[20:21], v19, off offset:3584
	global_load_dwordx4 v[10:13], v[136:137], off
	v_lshlrev_b32_e32 v14, 16, v42
	v_and_b32_e32 v15, 0xffff0000, v42
	v_mov_b32_e32 v19, v127
	v_lshlrev_b32_e32 v16, 16, v43
	v_and_b32_e32 v17, 0xffff0000, v43
	v_lshlrev_b32_e32 v22, 16, v6
	v_and_b32_e32 v23, 0xffff0000, v6
	v_pk_mul_f32 v[14:15], v[8:9], v[14:15] op_sel_hi:[0,1]
	v_lshlrev_b32_e32 v6, 16, v7
	v_and_b32_e32 v7, 0xffff0000, v7
	v_pk_mul_f32 v[8:9], v[8:9], v[16:17] op_sel_hi:[0,1]
	v_pk_mul_f32 v[16:17], v[18:19], v[22:23] op_sel_hi:[0,1]
	v_mov_b32_e32 v24, v127
	v_pk_mul_f32 v[6:7], v[18:19], v[6:7] op_sel_hi:[0,1]
	s_waitcnt vmcnt(0)
	v_pk_mul_f32 v[14:15], v[14:15], v[10:11]
	v_pk_mul_f32 v[10:11], v[16:17], v[10:11]
	v_cvt_pk_fp8_f32 v19, v14, v15
	v_cvt_pk_fp8_f32 v24, v10, v11
	v_pk_mul_f32 v[8:9], v[8:9], v[12:13]
	v_pk_mul_f32 v[6:7], v[6:7], v[12:13]
	v_cvt_pk_fp8_f32 v19, v8, v9 op_sel:[0,0,1]
	v_cvt_pk_fp8_f32 v24, v6, v7 op_sel:[0,0,1]
	v_lshl_add_u64 v[8:9], s[8:9], 0, v[126:127]
	global_store_dword v[20:21], v19, off offset:1792
	global_store_dword v[20:21], v24, off offset:3840
	global_load_dwordx2 v[10:11], v126, s[8:9]
	v_add_co_u32_e32 v6, vcc, s75, v8
	s_waitcnt vmcnt(0)
	v_lshlrev_b32_e32 v22, 16, v10
	v_addc_co_u32_e32 v7, vcc, 0, v9, vcc
	global_load_dwordx2 v[14:15], v[6:7], off
	global_load_dwordx4 v[18:21], v[128:129], off
	v_and_b32_e32 v23, 0xffff0000, v10
	s_waitcnt lgkmcnt(0)
	v_pk_mul_f32 v[22:23], v[2:3], v[22:23] op_sel_hi:[0,1]
	v_lshlrev_b32_e32 v10, 16, v11
	v_and_b32_e32 v11, 0xffff0000, v11
	v_pk_mul_f32 v[10:11], v[2:3], v[10:11] op_sel_hi:[0,1]
	v_lshl_add_u64 v[6:7], v[138:139], 0, s[10:11]
	v_lshl_add_u64 v[8:9], v[8:9], 0, s[42:43]
	global_load_dwordx2 v[24:25], v126, s[8:9] offset:512
	global_load_dwordx2 v[26:27], v126, s[8:9] offset:1024
	global_load_dwordx2 v[28:29], v126, s[8:9] offset:1536
	global_load_dwordx2 v[30:31], v[8:9], off offset:512
	global_load_dwordx2 v[32:33], v[8:9], off offset:1024
	global_load_dwordx2 v[34:35], v[8:9], off offset:1536
	global_load_dwordx2 v[36:37], v[8:9], off offset:2048
	global_load_dwordx2 v[16:17], v[8:9], off offset:2560
	global_load_dwordx2 v[12:13], v[8:9], off offset:3072
	s_nop 0
	global_load_dwordx2 v[8:9], v[8:9], off offset:3584
	s_add_i32 s10, s78, s58
	s_ashr_i32 s11, s10, 31
	s_waitcnt vmcnt(11)
	v_lshlrev_b32_e32 v38, 16, v14
	v_and_b32_e32 v39, 0xffff0000, v14
	v_pk_mul_f32 v[38:39], v[2:3], v[38:39] op_sel:[1,0]
	s_waitcnt vmcnt(10)
	v_pk_mul_f32 v[22:23], v[22:23], v[18:19]
	v_pk_mul_f32 v[18:19], v[38:39], v[18:19]
	v_cvt_pk_fp8_f32 v40, v22, v23
	v_cvt_pk_fp8_f32 v41, v18, v19
	v_lshlrev_b32_e32 v14, 16, v15
	v_and_b32_e32 v15, 0xffff0000, v15
	v_pk_mul_f32 v[14:15], v[2:3], v[14:15] op_sel:[1,0]
	v_pk_mul_f32 v[10:11], v[10:11], v[20:21]
	v_pk_mul_f32 v[14:15], v[14:15], v[20:21]
	v_cvt_pk_fp8_f32 v40, v10, v11 op_sel:[0,0,1]
	v_cvt_pk_fp8_f32 v41, v14, v15 op_sel:[0,0,1]
	global_load_dwordx2 v[38:39], v126, s[8:9] offset:2048
	global_load_dwordx2 v[18:19], v126, s[8:9] offset:2560
	global_load_dwordx2 v[14:15], v126, s[8:9] offset:3072
	global_load_dwordx2 v[10:11], v126, s[8:9] offset:3584
	s_nop 0
	global_store_dword v[6:7], v40, off
	global_store_dword v[6:7], v41, off offset:2048
	global_load_dwordx4 v[20:23], v[128:129], off offset:1024
	s_waitcnt vmcnt(16)
	v_lshlrev_b32_e32 v40, 16, v24
	v_and_b32_e32 v41, 0xffff0000, v24
	s_waitcnt vmcnt(13)
	v_lshlrev_b32_e32 v42, 16, v30
	v_and_b32_e32 v43, 0xffff0000, v30
	v_pk_mul_f32 v[40:41], v[2:3], v[40:41] op_sel_hi:[0,1]
	v_pk_mul_f32 v[42:43], v[2:3], v[42:43] op_sel:[1,0]
	v_lshlrev_b32_e32 v24, 16, v25
	v_and_b32_e32 v25, 0xffff0000, v25
	v_lshlrev_b32_e32 v30, 16, v31
	v_and_b32_e32 v31, 0xffff0000, v31
	v_pk_mul_f32 v[24:25], v[2:3], v[24:25] op_sel_hi:[0,1]
	v_pk_mul_f32 v[30:31], v[2:3], v[30:31] op_sel:[1,0]
	s_lshl_b64 s[8:9], s[10:11], 12
	s_add_u32 s8, s52, s8
	s_addc_u32 s9, s53, s9
	s_lshl_b64 s[10:11], s[10:11], 11
	s_waitcnt vmcnt(0)
	v_pk_mul_f32 v[40:41], v[40:41], v[20:21]
	v_pk_mul_f32 v[20:21], v[42:43], v[20:21]
	v_cvt_pk_fp8_f32 v44, v40, v41
	v_cvt_pk_fp8_f32 v45, v20, v21
	v_pk_mul_f32 v[20:21], v[24:25], v[22:23]
	v_pk_mul_f32 v[22:23], v[30:31], v[22:23]
	v_cvt_pk_fp8_f32 v44, v20, v21 op_sel:[0,0,1]
	v_cvt_pk_fp8_f32 v45, v22, v23 op_sel:[0,0,1]
	global_store_dword v[6:7], v44, off offset:256
	global_store_dword v[6:7], v45, off offset:2304
	global_load_dwordx4 v[20:23], v[128:129], off offset:2048
	v_lshlrev_b32_e32 v24, 16, v26
	v_and_b32_e32 v25, 0xffff0000, v26
	v_lshlrev_b32_e32 v30, 16, v32
	v_and_b32_e32 v31, 0xffff0000, v32
	v_pk_mul_f32 v[24:25], v[2:3], v[24:25] op_sel_hi:[0,1]
	v_mov_b32_e32 v40, v127
	v_pk_mul_f32 v[30:31], v[2:3], v[30:31] op_sel:[1,0]
	v_mov_b32_e32 v41, v127
	v_lshlrev_b32_e32 v26, 16, v27
	v_and_b32_e32 v27, 0xffff0000, v27
	v_lshlrev_b32_e32 v32, 16, v33
	v_and_b32_e32 v33, 0xffff0000, v33
	v_pk_mul_f32 v[26:27], v[2:3], v[26:27] op_sel_hi:[0,1]
	v_pk_mul_f32 v[32:33], v[2:3], v[32:33] op_sel:[1,0]
	s_waitcnt vmcnt(0)
	v_pk_mul_f32 v[24:25], v[24:25], v[20:21]
	v_pk_mul_f32 v[20:21], v[30:31], v[20:21]
	v_cvt_pk_fp8_f32 v40, v24, v25
	v_cvt_pk_fp8_f32 v41, v20, v21
	v_pk_mul_f32 v[20:21], v[26:27], v[22:23]
	v_pk_mul_f32 v[22:23], v[32:33], v[22:23]
	v_cvt_pk_fp8_f32 v40, v20, v21 op_sel:[0,0,1]
	v_cvt_pk_fp8_f32 v41, v22, v23 op_sel:[0,0,1]
	global_store_dword v[6:7], v40, off offset:512
	global_store_dword v[6:7], v41, off offset:2560
	global_load_dwordx4 v[20:23], v[128:129], off offset:3072
	v_lshlrev_b32_e32 v24, 16, v28
	v_and_b32_e32 v25, 0xffff0000, v28
	v_lshlrev_b32_e32 v26, 16, v29
	v_and_b32_e32 v27, 0xffff0000, v29
	v_lshlrev_b32_e32 v28, 16, v34
	v_and_b32_e32 v29, 0xffff0000, v34
	v_pk_mul_f32 v[24:25], v[2:3], v[24:25] op_sel_hi:[0,1]
	v_mov_b32_e32 v32, v127
	v_pk_mul_f32 v[28:29], v[2:3], v[28:29] op_sel:[1,0]
	v_mov_b32_e32 v33, v127
	v_lshlrev_b32_e32 v30, 16, v35
	v_and_b32_e32 v31, 0xffff0000, v35
	v_pk_mul_f32 v[26:27], v[2:3], v[26:27] op_sel_hi:[0,1]
	v_pk_mul_f32 v[30:31], v[2:3], v[30:31] op_sel:[1,0]
	v_mov_b32_e32 v40, v127
	s_waitcnt vmcnt(0)
	v_pk_mul_f32 v[24:25], v[24:25], v[20:21]
	v_pk_mul_f32 v[20:21], v[28:29], v[20:21]
	v_cvt_pk_fp8_f32 v32, v24, v25
	v_cvt_pk_fp8_f32 v33, v20, v21
	v_pk_mul_f32 v[20:21], v[26:27], v[22:23]
	v_pk_mul_f32 v[22:23], v[30:31], v[22:23]
	v_cvt_pk_fp8_f32 v32, v20, v21 op_sel:[0,0,1]
	v_cvt_pk_fp8_f32 v33, v22, v23 op_sel:[0,0,1]
	global_store_dword v[6:7], v32, off offset:768
	global_store_dword v[6:7], v33, off offset:2816
	global_load_dwordx4 v[20:23], v[130:131], off
	v_lshlrev_b32_e32 v24, 16, v38
	v_and_b32_e32 v25, 0xffff0000, v38
	v_lshlrev_b32_e32 v28, 16, v36
	v_and_b32_e32 v29, 0xffff0000, v36
	v_pk_mul_f32 v[24:25], v[2:3], v[24:25] op_sel_hi:[0,1]
	v_mov_b32_e32 v32, v127
	v_pk_mul_f32 v[28:29], v[2:3], v[28:29] op_sel:[1,0]
	v_mov_b32_e32 v33, v127
	v_lshlrev_b32_e32 v26, 16, v39
	v_and_b32_e32 v27, 0xffff0000, v39
	v_lshlrev_b32_e32 v30, 16, v37
	v_and_b32_e32 v31, 0xffff0000, v37
	v_pk_mul_f32 v[26:27], v[2:3], v[26:27] op_sel_hi:[0,1]
	v_pk_mul_f32 v[30:31], v[2:3], v[30:31] op_sel:[1,0]
	s_waitcnt vmcnt(0)
	v_pk_mul_f32 v[24:25], v[24:25], v[20:21]
	v_pk_mul_f32 v[20:21], v[28:29], v[20:21]
	v_cvt_pk_fp8_f32 v32, v24, v25
	v_cvt_pk_fp8_f32 v33, v20, v21
	v_pk_mul_f32 v[20:21], v[26:27], v[22:23]
	v_pk_mul_f32 v[22:23], v[30:31], v[22:23]
	v_cvt_pk_fp8_f32 v32, v20, v21 op_sel:[0,0,1]
	v_cvt_pk_fp8_f32 v33, v22, v23 op_sel:[0,0,1]
	global_store_dword v[6:7], v32, off offset:1024
	global_store_dword v[6:7], v33, off offset:3072
	global_load_dwordx4 v[20:23], v[132:133], off
	v_lshlrev_b32_e32 v24, 16, v18
	v_and_b32_e32 v25, 0xffff0000, v18
	v_lshlrev_b32_e32 v26, 16, v16
	v_and_b32_e32 v27, 0xffff0000, v16
	v_pk_mul_f32 v[24:25], v[2:3], v[24:25] op_sel_hi:[0,1]
	v_mov_b32_e32 v28, v127
	v_pk_mul_f32 v[26:27], v[2:3], v[26:27] op_sel:[1,0]
	v_mov_b32_e32 v29, v127
	v_lshlrev_b32_e32 v18, 16, v19
	v_and_b32_e32 v19, 0xffff0000, v19
	v_lshlrev_b32_e32 v16, 16, v17
	v_and_b32_e32 v17, 0xffff0000, v17
	v_pk_mul_f32 v[18:19], v[2:3], v[18:19] op_sel_hi:[0,1]
	v_pk_mul_f32 v[16:17], v[2:3], v[16:17] op_sel:[1,0]
	s_waitcnt vmcnt(0)
	v_pk_mul_f32 v[24:25], v[24:25], v[20:21]
	v_pk_mul_f32 v[20:21], v[26:27], v[20:21]
	v_cvt_pk_fp8_f32 v28, v24, v25
	v_cvt_pk_fp8_f32 v29, v20, v21
	v_pk_mul_f32 v[18:19], v[18:19], v[22:23]
	v_pk_mul_f32 v[16:17], v[16:17], v[22:23]
	v_cvt_pk_fp8_f32 v28, v18, v19 op_sel:[0,0,1]
	v_cvt_pk_fp8_f32 v29, v16, v17 op_sel:[0,0,1]
	global_store_dword v[6:7], v28, off offset:1280
	global_store_dword v[6:7], v29, off offset:3328
	global_load_dwordx4 v[16:19], v[134:135], off
	v_lshlrev_b32_e32 v20, 16, v14
	v_and_b32_e32 v21, 0xffff0000, v14
	v_lshlrev_b32_e32 v22, 16, v12
	v_and_b32_e32 v23, 0xffff0000, v12
	v_pk_mul_f32 v[20:21], v[2:3], v[20:21] op_sel_hi:[0,1]
	v_mov_b32_e32 v24, v127
	v_pk_mul_f32 v[22:23], v[2:3], v[22:23] op_sel:[1,0]
	v_mov_b32_e32 v25, v127
	v_lshlrev_b32_e32 v14, 16, v15
	v_and_b32_e32 v15, 0xffff0000, v15
	v_lshlrev_b32_e32 v12, 16, v13
	v_and_b32_e32 v13, 0xffff0000, v13
	v_pk_mul_f32 v[14:15], v[2:3], v[14:15] op_sel_hi:[0,1]
	v_pk_mul_f32 v[12:13], v[2:3], v[12:13] op_sel:[1,0]
	s_waitcnt vmcnt(0)
	v_pk_mul_f32 v[20:21], v[20:21], v[16:17]
	v_pk_mul_f32 v[16:17], v[22:23], v[16:17]
	v_cvt_pk_fp8_f32 v24, v20, v21
	v_cvt_pk_fp8_f32 v25, v16, v17
	v_pk_mul_f32 v[14:15], v[14:15], v[18:19]
	v_pk_mul_f32 v[12:13], v[12:13], v[18:19]
	v_cvt_pk_fp8_f32 v24, v14, v15 op_sel:[0,0,1]
	v_cvt_pk_fp8_f32 v25, v12, v13 op_sel:[0,0,1]
	global_store_dword v[6:7], v24, off offset:1536
	global_store_dword v[6:7], v25, off offset:3584
	global_load_dwordx4 v[12:15], v[136:137], off
	v_lshlrev_b32_e32 v16, 16, v10
	v_and_b32_e32 v17, 0xffff0000, v10
	v_lshlrev_b32_e32 v10, 16, v11
	v_and_b32_e32 v11, 0xffff0000, v11
	v_lshlrev_b32_e32 v18, 16, v8
	v_and_b32_e32 v19, 0xffff0000, v8
	v_lshlrev_b32_e32 v8, 16, v9
	v_and_b32_e32 v9, 0xffff0000, v9
	v_pk_mul_f32 v[16:17], v[2:3], v[16:17] op_sel_hi:[0,1]
	v_mov_b32_e32 v20, v127
	v_pk_mul_f32 v[10:11], v[2:3], v[10:11] op_sel_hi:[0,1]
	v_pk_mul_f32 v[18:19], v[2:3], v[18:19] op_sel:[1,0]
	v_pk_mul_f32 v[2:3], v[2:3], v[8:9] op_sel:[1,0]
	v_mov_b32_e32 v21, v127
	s_waitcnt vmcnt(0)
	v_pk_mul_f32 v[8:9], v[16:17], v[12:13]
	v_pk_mul_f32 v[12:13], v[18:19], v[12:13]
	v_cvt_pk_fp8_f32 v20, v8, v9
	v_cvt_pk_fp8_f32 v21, v12, v13
	v_pk_mul_f32 v[8:9], v[10:11], v[14:15]
	v_pk_mul_f32 v[2:3], v[2:3], v[14:15]
	v_cvt_pk_fp8_f32 v20, v8, v9 op_sel:[0,0,1]
	v_cvt_pk_fp8_f32 v21, v2, v3 op_sel:[0,0,1]
	v_lshl_add_u64 v[8:9], s[8:9], 0, v[126:127]
	global_store_dword v[6:7], v20, off offset:1792
	global_store_dword v[6:7], v21, off offset:3840
	global_load_dwordx2 v[10:11], v126, s[8:9]
	v_add_co_u32_e32 v2, vcc, s75, v8
	v_mov_b32_e32 v7, v127
	s_nop 0
	v_addc_co_u32_e32 v3, vcc, 0, v9, vcc
	global_load_dwordx2 v[14:15], v[2:3], off
	global_load_dwordx4 v[18:21], v[128:129], off
	v_mov_b32_e32 v6, v5
	v_lshl_add_u64 v[2:3], v[138:139], 0, s[10:11]
	v_lshl_add_u64 v[8:9], v[8:9], 0, s[42:43]
	global_load_dwordx2 v[24:25], v126, s[8:9] offset:512
	global_load_dwordx2 v[26:27], v126, s[8:9] offset:1024
	global_load_dwordx2 v[28:29], v126, s[8:9] offset:1536
	global_load_dwordx2 v[30:31], v[8:9], off offset:512
	global_load_dwordx2 v[32:33], v[8:9], off offset:1024
	global_load_dwordx2 v[34:35], v[8:9], off offset:1536
	global_load_dwordx2 v[36:37], v[8:9], off offset:2048
	global_load_dwordx2 v[16:17], v[8:9], off offset:2560
	global_load_dwordx2 v[12:13], v[8:9], off offset:3072
	s_nop 0
	global_load_dwordx2 v[8:9], v[8:9], off offset:3584
	s_waitcnt vmcnt(12)
	v_lshlrev_b32_e32 v22, 16, v10
	v_and_b32_e32 v23, 0xffff0000, v10
	v_pk_mul_f32 v[22:23], v[4:5], v[22:23] op_sel_hi:[0,1]
	v_lshlrev_b32_e32 v10, 16, v11
	v_and_b32_e32 v11, 0xffff0000, v11
	s_waitcnt vmcnt(11)
	v_lshlrev_b32_e32 v38, 16, v14
	v_and_b32_e32 v39, 0xffff0000, v14
	v_lshlrev_b32_e32 v14, 16, v15
	v_and_b32_e32 v15, 0xffff0000, v15
	v_pk_mul_f32 v[38:39], v[6:7], v[38:39] op_sel_hi:[0,1]
	s_waitcnt vmcnt(10)
	v_pk_mul_f32 v[22:23], v[22:23], v[18:19]
	v_pk_mul_f32 v[14:15], v[6:7], v[14:15] op_sel_hi:[0,1]
	v_pk_mul_f32 v[18:19], v[38:39], v[18:19]
	v_cvt_pk_fp8_f32 v7, v22, v23
	v_cvt_pk_fp8_f32 v40, v18, v19
	v_pk_mul_f32 v[10:11], v[4:5], v[10:11] op_sel_hi:[0,1]
	v_pk_mul_f32 v[10:11], v[10:11], v[20:21]
	v_pk_mul_f32 v[14:15], v[14:15], v[20:21]
	v_cvt_pk_fp8_f32 v7, v10, v11 op_sel:[0,0,1]
	v_cvt_pk_fp8_f32 v40, v14, v15 op_sel:[0,0,1]
	global_load_dwordx2 v[38:39], v126, s[8:9] offset:2048
	global_load_dwordx2 v[18:19], v126, s[8:9] offset:2560
	global_load_dwordx2 v[14:15], v126, s[8:9] offset:3072
	global_load_dwordx2 v[10:11], v126, s[8:9] offset:3584
	s_nop 0
	global_store_dword v[2:3], v7, off
	global_store_dword v[2:3], v40, off offset:2048
	global_load_dwordx4 v[20:23], v[128:129], off offset:1024
	v_mov_b32_e32 v5, v127
	s_waitcnt vmcnt(16)
	v_lshlrev_b32_e32 v40, 16, v24
	v_and_b32_e32 v41, 0xffff0000, v24
	v_mov_b32_e32 v7, v127
	s_waitcnt vmcnt(13)
	v_lshlrev_b32_e32 v42, 16, v30
	v_and_b32_e32 v43, 0xffff0000, v30
	v_pk_mul_f32 v[40:41], v[4:5], v[40:41] op_sel_hi:[0,1]
	v_lshlrev_b32_e32 v24, 16, v25
	v_and_b32_e32 v25, 0xffff0000, v25
	v_pk_mul_f32 v[42:43], v[6:7], v[42:43] op_sel_hi:[0,1]
	v_lshlrev_b32_e32 v30, 16, v31
	v_and_b32_e32 v31, 0xffff0000, v31
	v_pk_mul_f32 v[24:25], v[4:5], v[24:25] op_sel_hi:[0,1]
	v_pk_mul_f32 v[30:31], v[6:7], v[30:31] op_sel_hi:[0,1]
	s_waitcnt vmcnt(0)
	v_pk_mul_f32 v[40:41], v[40:41], v[20:21]
	v_pk_mul_f32 v[20:21], v[42:43], v[20:21]
	v_cvt_pk_fp8_f32 v5, v40, v41
	v_cvt_pk_fp8_f32 v7, v20, v21
	v_pk_mul_f32 v[20:21], v[24:25], v[22:23]
	v_pk_mul_f32 v[22:23], v[30:31], v[22:23]
	v_cvt_pk_fp8_f32 v5, v20, v21 op_sel:[0,0,1]
	v_cvt_pk_fp8_f32 v7, v22, v23 op_sel:[0,0,1]
	global_store_dword v[2:3], v5, off offset:256
	global_store_dword v[2:3], v7, off offset:2304
	global_load_dwordx4 v[20:23], v[128:129], off offset:2048
	v_mov_b32_e32 v5, v127
	v_lshlrev_b32_e32 v24, 16, v26
	v_and_b32_e32 v25, 0xffff0000, v26
	v_mov_b32_e32 v7, v127
	v_lshlrev_b32_e32 v30, 16, v32
	v_and_b32_e32 v31, 0xffff0000, v32
	v_pk_mul_f32 v[24:25], v[4:5], v[24:25] op_sel_hi:[0,1]
	v_lshlrev_b32_e32 v26, 16, v27
	v_and_b32_e32 v27, 0xffff0000, v27
	v_pk_mul_f32 v[30:31], v[6:7], v[30:31] op_sel_hi:[0,1]
	v_lshlrev_b32_e32 v32, 16, v33
	v_and_b32_e32 v33, 0xffff0000, v33
	v_pk_mul_f32 v[26:27], v[4:5], v[26:27] op_sel_hi:[0,1]
	v_pk_mul_f32 v[32:33], v[6:7], v[32:33] op_sel_hi:[0,1]
	s_waitcnt vmcnt(0)
	v_pk_mul_f32 v[24:25], v[24:25], v[20:21]
	v_pk_mul_f32 v[20:21], v[30:31], v[20:21]
	v_cvt_pk_fp8_f32 v5, v24, v25
	v_cvt_pk_fp8_f32 v7, v20, v21
	v_pk_mul_f32 v[20:21], v[26:27], v[22:23]
	v_pk_mul_f32 v[22:23], v[32:33], v[22:23]
	v_cvt_pk_fp8_f32 v5, v20, v21 op_sel:[0,0,1]
	v_cvt_pk_fp8_f32 v7, v22, v23 op_sel:[0,0,1]
	global_store_dword v[2:3], v5, off offset:512
	global_store_dword v[2:3], v7, off offset:2560
	global_load_dwordx4 v[20:23], v[128:129], off offset:3072
	v_mov_b32_e32 v5, v127
	v_lshlrev_b32_e32 v24, 16, v28
	v_and_b32_e32 v25, 0xffff0000, v28
	v_mov_b32_e32 v7, v127
	v_lshlrev_b32_e32 v26, 16, v29
	v_and_b32_e32 v27, 0xffff0000, v29
	v_lshlrev_b32_e32 v28, 16, v34
	v_and_b32_e32 v29, 0xffff0000, v34
	v_pk_mul_f32 v[24:25], v[4:5], v[24:25] op_sel_hi:[0,1]
	v_pk_mul_f32 v[28:29], v[6:7], v[28:29] op_sel_hi:[0,1]
	v_lshlrev_b32_e32 v30, 16, v35
	v_and_b32_e32 v31, 0xffff0000, v35
	v_pk_mul_f32 v[26:27], v[4:5], v[26:27] op_sel_hi:[0,1]
	v_pk_mul_f32 v[30:31], v[6:7], v[30:31] op_sel_hi:[0,1]
	s_waitcnt vmcnt(0)
	v_pk_mul_f32 v[24:25], v[24:25], v[20:21]
	v_pk_mul_f32 v[20:21], v[28:29], v[20:21]
	v_cvt_pk_fp8_f32 v5, v24, v25
	v_cvt_pk_fp8_f32 v7, v20, v21
	v_pk_mul_f32 v[20:21], v[26:27], v[22:23]
	v_pk_mul_f32 v[22:23], v[30:31], v[22:23]
	v_cvt_pk_fp8_f32 v5, v20, v21 op_sel:[0,0,1]
	v_cvt_pk_fp8_f32 v7, v22, v23 op_sel:[0,0,1]
	global_store_dword v[2:3], v5, off offset:768
	global_store_dword v[2:3], v7, off offset:2816
	global_load_dwordx4 v[20:23], v[130:131], off
	v_mov_b32_e32 v5, v127
	v_lshlrev_b32_e32 v24, 16, v38
	v_and_b32_e32 v25, 0xffff0000, v38
	v_mov_b32_e32 v7, v127
	v_lshlrev_b32_e32 v28, 16, v36
	v_and_b32_e32 v29, 0xffff0000, v36
	v_pk_mul_f32 v[24:25], v[4:5], v[24:25] op_sel_hi:[0,1]
	v_lshlrev_b32_e32 v26, 16, v39
	v_and_b32_e32 v27, 0xffff0000, v39
	v_pk_mul_f32 v[28:29], v[6:7], v[28:29] op_sel_hi:[0,1]
	v_lshlrev_b32_e32 v30, 16, v37
	v_and_b32_e32 v31, 0xffff0000, v37
	v_pk_mul_f32 v[26:27], v[4:5], v[26:27] op_sel_hi:[0,1]
	v_pk_mul_f32 v[30:31], v[6:7], v[30:31] op_sel_hi:[0,1]
	s_waitcnt vmcnt(0)
	v_pk_mul_f32 v[24:25], v[24:25], v[20:21]
	v_pk_mul_f32 v[20:21], v[28:29], v[20:21]
	v_cvt_pk_fp8_f32 v5, v24, v25
	v_cvt_pk_fp8_f32 v7, v20, v21
	v_pk_mul_f32 v[20:21], v[26:27], v[22:23]
	v_pk_mul_f32 v[22:23], v[30:31], v[22:23]
	v_cvt_pk_fp8_f32 v5, v20, v21 op_sel:[0,0,1]
	v_cvt_pk_fp8_f32 v7, v22, v23 op_sel:[0,0,1]
	global_store_dword v[2:3], v5, off offset:1024
	global_store_dword v[2:3], v7, off offset:3072
	global_load_dwordx4 v[20:23], v[132:133], off
	v_mov_b32_e32 v5, v127
	v_lshlrev_b32_e32 v24, 16, v18
	v_and_b32_e32 v25, 0xffff0000, v18
	v_mov_b32_e32 v7, v127
	v_lshlrev_b32_e32 v26, 16, v16
	v_and_b32_e32 v27, 0xffff0000, v16
	v_pk_mul_f32 v[24:25], v[4:5], v[24:25] op_sel_hi:[0,1]
	v_lshlrev_b32_e32 v18, 16, v19
	v_and_b32_e32 v19, 0xffff0000, v19
	v_pk_mul_f32 v[26:27], v[6:7], v[26:27] op_sel_hi:[0,1]
	v_lshlrev_b32_e32 v16, 16, v17
	v_and_b32_e32 v17, 0xffff0000, v17
	v_pk_mul_f32 v[18:19], v[4:5], v[18:19] op_sel_hi:[0,1]
	v_pk_mul_f32 v[16:17], v[6:7], v[16:17] op_sel_hi:[0,1]
	s_waitcnt vmcnt(0)
	v_pk_mul_f32 v[24:25], v[24:25], v[20:21]
	v_pk_mul_f32 v[20:21], v[26:27], v[20:21]
	v_cvt_pk_fp8_f32 v5, v24, v25
	v_cvt_pk_fp8_f32 v7, v20, v21
	v_pk_mul_f32 v[18:19], v[18:19], v[22:23]
	v_pk_mul_f32 v[16:17], v[16:17], v[22:23]
	v_cvt_pk_fp8_f32 v5, v18, v19 op_sel:[0,0,1]
	v_cvt_pk_fp8_f32 v7, v16, v17 op_sel:[0,0,1]
	global_store_dword v[2:3], v5, off offset:1280
	global_store_dword v[2:3], v7, off offset:3328
	global_load_dwordx4 v[16:19], v[134:135], off
	v_mov_b32_e32 v5, v127
	v_lshlrev_b32_e32 v20, 16, v14
	v_and_b32_e32 v21, 0xffff0000, v14
	v_mov_b32_e32 v7, v127
	v_lshlrev_b32_e32 v22, 16, v12
	v_and_b32_e32 v23, 0xffff0000, v12
	v_pk_mul_f32 v[20:21], v[4:5], v[20:21] op_sel_hi:[0,1]
	v_lshlrev_b32_e32 v14, 16, v15
	v_and_b32_e32 v15, 0xffff0000, v15
	v_pk_mul_f32 v[22:23], v[6:7], v[22:23] op_sel_hi:[0,1]
	v_lshlrev_b32_e32 v12, 16, v13
	v_and_b32_e32 v13, 0xffff0000, v13
	v_pk_mul_f32 v[14:15], v[4:5], v[14:15] op_sel_hi:[0,1]
	v_pk_mul_f32 v[12:13], v[6:7], v[12:13] op_sel_hi:[0,1]
	s_waitcnt vmcnt(0)
	v_pk_mul_f32 v[20:21], v[20:21], v[16:17]
	v_pk_mul_f32 v[16:17], v[22:23], v[16:17]
	v_cvt_pk_fp8_f32 v5, v20, v21
	v_cvt_pk_fp8_f32 v7, v16, v17
	v_pk_mul_f32 v[14:15], v[14:15], v[18:19]
	v_pk_mul_f32 v[12:13], v[12:13], v[18:19]
	v_cvt_pk_fp8_f32 v5, v14, v15 op_sel:[0,0,1]
	v_cvt_pk_fp8_f32 v7, v12, v13 op_sel:[0,0,1]
	global_store_dword v[2:3], v5, off offset:1536
	global_store_dword v[2:3], v7, off offset:3584
	global_load_dwordx4 v[12:15], v[136:137], off
	v_lshlrev_b32_e32 v16, 16, v10
	v_and_b32_e32 v17, 0xffff0000, v10
	v_lshlrev_b32_e32 v10, 16, v11
	v_and_b32_e32 v11, 0xffff0000, v11
	v_lshlrev_b32_e32 v18, 16, v8
	v_and_b32_e32 v19, 0xffff0000, v8
	v_lshlrev_b32_e32 v8, 16, v9
	v_and_b32_e32 v9, 0xffff0000, v9
	v_pk_mul_f32 v[16:17], v[4:5], v[16:17] op_sel_hi:[0,1]
	v_mov_b32_e32 v20, v127
	v_pk_mul_f32 v[4:5], v[4:5], v[10:11] op_sel_hi:[0,1]
	v_pk_mul_f32 v[10:11], v[6:7], v[18:19] op_sel_hi:[0,1]
	v_pk_mul_f32 v[6:7], v[6:7], v[8:9] op_sel_hi:[0,1]
	v_mov_b32_e32 v21, v127
	s_waitcnt vmcnt(0)
	v_pk_mul_f32 v[8:9], v[16:17], v[12:13]
	v_pk_mul_f32 v[10:11], v[10:11], v[12:13]
	v_cvt_pk_fp8_f32 v20, v8, v9
	v_cvt_pk_fp8_f32 v21, v10, v11
	v_pk_mul_f32 v[4:5], v[4:5], v[14:15]
	v_pk_mul_f32 v[6:7], v[6:7], v[14:15]
	v_cvt_pk_fp8_f32 v20, v4, v5 op_sel:[0,0,1]
	v_cvt_pk_fp8_f32 v21, v6, v7 op_sel:[0,0,1]
	global_store_dword v[2:3], v20, off offset:1792
	global_store_dword v[2:3], v21, off offset:3840
	s_and_saveexec_b64 s[44:45], s[6:7]
	s_cbranch_execz .LBB0_909
	v_mov_b32_e32 v18, 0
	global_load_dwordx4 v[6:9], v18, s[14:15]
	global_load_dwordx4 v[2:5], v18, s[14:15] offset:16
	ds_read_b32 v17, v155 offset:20736
	ds_read_b128 v[12:15], v156
	ds_read_b128 v[20:23], v156 offset:16
	v_mov_b32_e32 v11, v127
	s_waitcnt vmcnt(1) lgkmcnt(1)
	v_fma_f32 v12, v17, v12, v6
	v_fma_f32 v13, v17, v13, v7
	v_fma_f32 v8, v17, v14, v8
	s_waitcnt vmcnt(0) lgkmcnt(0)
	v_fma_f32 v14, v17, v20, v2
	v_max_f32_e32 v2, 0xff800000, v12
	v_cmp_gt_f32_e32 vcc, v13, v2
	v_fmac_f32_e32 v9, v17, v15
	v_fma_f32 v15, v17, v21, v3
	v_cndmask_b32_e32 v2, v2, v13, vcc
	v_cmp_gt_f32_e64 s[8:9], v8, v2
	v_cndmask_b32_e64 v3, 0, 8, vcc
	v_fma_f32 v4, v17, v22, v4
	v_cndmask_b32_e64 v2, v2, v8, s[8:9]
	v_cmp_gt_f32_e32 vcc, v9, v2
	v_cndmask_b32_e64 v3, v3, 16, s[8:9]
	v_fmac_f32_e32 v5, v17, v23
	v_cndmask_b32_e32 v2, v2, v9, vcc
	v_cmp_gt_f32_e64 s[8:9], v14, v2
	v_cndmask_b32_e64 v3, v3, 24, vcc
	s_nop 0
	v_cndmask_b32_e64 v2, v2, v14, s[8:9]
	v_cmp_gt_f32_e32 vcc, v15, v2
	v_cndmask_b32_e64 v3, v3, 32, s[8:9]
	s_nop 0
	v_cndmask_b32_e32 v2, v2, v15, vcc
	v_cmp_gt_f32_e64 s[8:9], v4, v2
	s_nop 1
	v_cndmask_b32_e64 v16, v2, v4, s[8:9]
	v_cndmask_b32_e64 v2, v3, 40, vcc
	v_cndmask_b32_e64 v2, v2, 48, s[8:9]
	v_cmp_gt_f32_e32 vcc, v5, v16
	s_nop 1
	v_cndmask_b32_e64 v10, v2, 56, vcc
	v_lshl_add_u64 v[2:3], v[10:11], 2, s[16:17]
	global_load_dwordx4 v[246:249], v[2:3], off
	global_load_dwordx4 v[250:253], v[2:3], off offset:16
	v_lshl_add_u32 v11, v10, 2, v156
	ds_read2_b32 v[20:21], v11 offset0:8 offset1:9
	s_waitcnt vmcnt(0) lgkmcnt(0)
	v_mov_b32_e32 v6, v246
	v_mov_b32_e32 v7, v247
	v_fma_f32 v6, v17, v20, v6
	v_cmp_lg_f32_e64 s[8:9], s76, v6
	v_fmac_f32_e32 v7, v17, v21
	s_nop 0
	v_cndmask_b32_e64 v20, v163, v6, s[8:9]
	v_cmp_ngt_f32_e64 s[8:9], v7, v20
	v_mov_b32_e32 v6, 1
	s_and_saveexec_b64 s[10:11], s[8:9]
	s_cbranch_execz .LBB0_941
	v_mov_b32_e32 v19, 0xff800000
	v_cmp_lg_f32_e64 s[8:9], v7, v19
	v_mov_b32_e32 v6, 0
	v_mov_b32_e32 v18, 0
	s_and_saveexec_b64 s[46:47], s[8:9]
	v_mov_b32_e32 v18, 1
	v_mov_b32_e32 v19, v7
	s_or_b64 exec, exec, s[46:47]
	v_mov_b32_e32 v7, v20
	v_mov_b32_e32 v20, v19
.LBB0_941:
	s_or_b64 exec, exec, s[10:11]
	v_mov_b32_e32 v19, v248
	ds_read_b32 v21, v11 offset:40
	s_waitcnt lgkmcnt(0)
	v_fmac_f32_e32 v19, v17, v21
	v_cmp_ngt_f32_e64 s[8:9], v19, v7
	v_mov_b32_e32 v21, 2
	s_and_saveexec_b64 s[10:11], s[8:9]
	s_cbranch_execz .LBB0_945
	v_cmp_gt_f32_e64 s[8:9], v19, v20
	s_and_saveexec_b64 s[46:47], s[8:9]
	v_mov_b32_e32 v18, 2
	v_mov_b32_e32 v20, v19
	s_or_b64 exec, exec, s[46:47]
	v_mov_b32_e32 v19, v7
	v_mov_b32_e32 v7, v20
	v_mov_b32_e32 v21, v6
	v_mov_b32_e32 v6, v18
.LBB0_945:
	s_or_b64 exec, exec, s[10:11]
	v_mov_b32_e32 v18, v249
	ds_read_b32 v20, v11 offset:44
	v_mov_b32_e32 v22, 3
	s_waitcnt lgkmcnt(0)
	v_fmac_f32_e32 v18, v17, v20
	v_cmp_ngt_f32_e64 s[8:9], v18, v19
	s_and_saveexec_b64 s[10:11], s[8:9]
	s_cbranch_execz .LBB0_949
	v_cmp_gt_f32_e64 s[8:9], v18, v7
	s_and_saveexec_b64 s[46:47], s[8:9]
	v_mov_b32_e32 v6, 3
	v_mov_b32_e32 v7, v18
	s_or_b64 exec, exec, s[46:47]
	v_mov_b32_e32 v18, v19
	v_mov_b32_e32 v19, v7
	v_mov_b32_e32 v22, v21
	v_mov_b32_e32 v21, v6
.LBB0_949:
	s_or_b64 exec, exec, s[10:11]
	v_mov_b32_e32 v20, v250
	ds_read_b32 v6, v11 offset:48
	v_mov_b32_e32 v23, 4
	s_waitcnt lgkmcnt(0)
	v_fmac_f32_e32 v20, v17, v6
	v_cmp_ngt_f32_e64 s[8:9], v20, v18
	s_and_saveexec_b64 s[10:11], s[8:9]
	s_cbranch_execz .LBB0_953
	v_cmp_gt_f32_e64 s[8:9], v20, v19
	s_and_saveexec_b64 s[46:47], s[8:9]
	v_mov_b32_e32 v21, 4
	v_mov_b32_e32 v19, v20
	s_or_b64 exec, exec, s[46:47]
	v_mov_b32_e32 v20, v18
	v_mov_b32_e32 v18, v19
	v_mov_b32_e32 v23, v22
	v_mov_b32_e32 v22, v21
.LBB0_953:
	s_or_b64 exec, exec, s[10:11]
	v_mov_b32_e32 v19, v251
	ds_read_b32 v6, v11 offset:52
	v_mov_b32_e32 v21, 5
	s_waitcnt lgkmcnt(0)
	v_fmac_f32_e32 v19, v17, v6
	v_cmp_ngt_f32_e64 s[8:9], v19, v20
	s_and_saveexec_b64 s[10:11], s[8:9]
	s_cbranch_execz .LBB0_957
	v_cmp_gt_f32_e64 s[8:9], v19, v18
	s_and_saveexec_b64 s[46:47], s[8:9]
	v_mov_b32_e32 v22, 5
	v_mov_b32_e32 v18, v19
	s_or_b64 exec, exec, s[46:47]
	v_mov_b32_e32 v19, v20
	v_mov_b32_e32 v20, v18
	v_mov_b32_e32 v21, v23
	v_mov_b32_e32 v23, v22
.LBB0_957:
	s_or_b64 exec, exec, s[10:11]
	v_mov_b32_e32 v6, v252
	ds_read_b32 v7, v11 offset:56
	s_waitcnt lgkmcnt(0)
	v_fmac_f32_e32 v6, v17, v7
	v_cmp_ngt_f32_e64 s[8:9], v6, v19
	v_mov_b32_e32 v7, 6
	s_and_saveexec_b64 s[10:11], s[8:9]
	s_cbranch_execz .LBB0_961
	v_cmp_gt_f32_e64 s[8:9], v6, v20
	s_and_saveexec_b64 s[46:47], s[8:9]
	v_mov_b32_e32 v23, 6
	v_mov_b32_e32 v20, v6
	s_or_b64 exec, exec, s[46:47]
	v_mov_b32_e32 v6, v19
	v_mov_b32_e32 v19, v20
	v_mov_b32_e32 v7, v21
	v_mov_b32_e32 v21, v23
.LBB0_961:
	s_or_b64 exec, exec, s[10:11]
	v_mov_b32_e32 v2, v253
	ds_read_b32 v3, v11 offset:60
	s_waitcnt lgkmcnt(0)
	v_fmac_f32_e32 v2, v17, v3
	v_cmp_ngt_f32_e64 s[8:9], v2, v6
	v_mov_b32_e32 v3, 7
	s_and_saveexec_b64 s[10:11], s[8:9]
	s_cbranch_execz .LBB0_908
	v_cmp_gt_f32_e64 s[8:9], v2, v19
	s_and_saveexec_b64 s[46:47], s[8:9]
	s_cbranch_execz .LBB0_907
	v_mov_b32_e32 v21, 7
	v_mov_b32_e32 v19, v2
	s_branch .LBB0_907

.Lplan_done:
.LBB0_1040:
	s_or_b64 exec, exec, s[4:5]
	s_add_i32 s4, 0, 0x24580
	v_mov_b32_e32 v1, s4
	s_waitcnt lgkmcnt(0)
	s_barrier
	ds_read_b32 v1, v1
	s_and_b32 s4, s2, 7
	s_ashr_i32 s5, s3, 3
	s_mul_i32 s44, s5, s4
	s_ashr_i32 s4, s2, 3
	s_waitcnt lgkmcnt(0)
	v_readfirstlane_b32 s45, v1
	s_andn2_b64 vcc, exec, s[10:11]
	s_add_i32 s44, s44, s4
	s_cbranch_vccnz .LBB0_1086
	s_mov_b64 s[74:75], 0
	s_mov_b64 s[76:77], 0
	s_mov_b64 s[78:79], 0
	s_mov_b64 s[80:81], 0
	s_mov_b64 s[82:83], 0
	s_load_dwordx2 s[6:7], s[0:1], 0xb0
	s_mul_i32 s25, s45, 6
	s_movk_i32 s4, 0x100
	v_cmp_gt_u32_e32 vcc, s4, v0
	s_mul_hi_i32 s19, s44, 0x2aaaaaab
	s_waitcnt lgkmcnt(0)
	s_add_u32 s12, s6, 0x3380a000
	s_addc_u32 s13, s7, 0
	s_add_i32 s18, 0, 0x24600
	s_cmp_lt_i32 s44, s25
	s_cselect_b64 s[8:9], -1, 0
	v_lshl_add_u32 v1, v0, 2, s18
	s_and_b64 s[4:5], s[8:9], vcc
	s_and_saveexec_b64 s[14:15], s[4:5]
	s_cbranch_execz .LBB0_1045
	s_lshr_b32 s4, s19, 31
	s_add_i32 s4, s19, s4
	s_lshl_b32 s5, s4, 2
	s_add_i32 s5, s5, 0
	s_add_i32 s5, s5, 0x24280
	s_waitcnt vmcnt(7)
	v_mov_b32_e32 v2, s5
	ds_read_b32 v2, v2
	s_waitcnt lgkmcnt(0)
	v_lshlrev_b32_e32 v3, 2, v2
	v_add_u32_e32 v3, 0, v3
	v_add_u32_e32 v4, 0x24140, v3
	ds_read_b32 v4, v4
	v_add_u32_e32 v3, 0x24040, v3
	ds_read_b32 v3, v3
	s_waitcnt lgkmcnt(1)
	v_sub_u32_e32 v4, s4, v4
	v_lshlrev_b32_e32 v4, 8, v4
	v_or_b32_e32 v5, v4, v0
	s_waitcnt lgkmcnt(0)
	v_cmp_lt_i32_e64 s[4:5], v5, v3
	v_mov_b32_e32 v3, 0
	v_mov_b32_e32 v10, 0
	s_and_saveexec_b64 s[16:17], s[4:5]
	s_cbranch_execz .LBB0_1044
	v_lshlrev_b32_e32 v2, 14, v2
	v_add_u32_e32 v2, v4, v2
	v_or_b32_e32 v2, v2, v0
	v_mov_b32_e32 v3, 0
	v_lshl_add_u64 v[2:3], v[2:3], 2, s[12:13]
	global_load_dword v10, v[2:3], off
.LBB0_1044:
	s_or_b64 exec, exec, s[16:17]
	s_mov_b64 s[74:75], exec
.LBB0_1045:
	s_or_b64 exec, exec, s[14:15]
	s_add_i32 s20, s3, s44
	s_cmp_lt_i32 s20, s25
	s_cselect_b64 s[4:5], -1, 0
	s_and_b64 s[4:5], s[4:5], vcc
	s_and_saveexec_b64 s[14:15], s[4:5]
	s_cbranch_execz .LBB0_1049
	s_mul_hi_i32 s4, s20, 0x2aaaaaab
	s_lshr_b32 s5, s4, 31
	s_add_i32 s4, s4, s5
	s_lshl_b32 s5, s4, 2
	s_add_i32 s5, s5, 0
	s_add_i32 s5, s5, 0x24280
	s_waitcnt vmcnt(7)
	v_mov_b32_e32 v2, s5
	ds_read_b32 v2, v2
	s_waitcnt lgkmcnt(0)
	v_lshlrev_b32_e32 v3, 2, v2
	v_add_u32_e32 v3, 0, v3
	v_add_u32_e32 v4, 0x24140, v3
	ds_read_b32 v4, v4
	v_add_u32_e32 v3, 0x24040, v3
	ds_read_b32 v3, v3
	s_waitcnt lgkmcnt(1)
	v_sub_u32_e32 v4, s4, v4
	v_lshlrev_b32_e32 v4, 8, v4
	v_or_b32_e32 v5, v4, v0
	s_waitcnt lgkmcnt(0)
	v_cmp_lt_i32_e64 s[4:5], v5, v3
	v_mov_b32_e32 v3, 0
	v_mov_b32_e32 v11, 0
	s_and_saveexec_b64 s[16:17], s[4:5]
	s_cbranch_execz .LBB0_1048
	v_lshlrev_b32_e32 v2, 14, v2
	v_add_u32_e32 v2, v4, v2
	v_or_b32_e32 v2, v2, v0
	v_mov_b32_e32 v3, 0
	v_lshl_add_u64 v[2:3], v[2:3], 2, s[12:13]
	global_load_dword v11, v[2:3], off
.LBB0_1048:
	s_or_b64 exec, exec, s[16:17]
	s_mov_b64 s[76:77], exec
.LBB0_1049:
	s_or_b64 exec, exec, s[14:15]
	s_add_i32 s20, s20, s3
	s_cmp_lt_i32 s20, s25
	s_cselect_b64 s[4:5], -1, 0
	s_and_b64 s[4:5], s[4:5], vcc
	s_and_saveexec_b64 s[14:15], s[4:5]
	s_cbranch_execz .LBB0_1053
	s_mul_hi_i32 s4, s20, 0x2aaaaaab
	s_lshr_b32 s5, s4, 31
	s_add_i32 s4, s4, s5
	s_lshl_b32 s5, s4, 2
	s_add_i32 s5, s5, 0
	s_add_i32 s5, s5, 0x24280
	s_waitcnt vmcnt(7)
	v_mov_b32_e32 v2, s5
	ds_read_b32 v2, v2
	s_waitcnt lgkmcnt(0)
	v_lshlrev_b32_e32 v3, 2, v2
	v_add_u32_e32 v3, 0, v3
	v_add_u32_e32 v4, 0x24140, v3
	ds_read_b32 v4, v4
	v_add_u32_e32 v3, 0x24040, v3
	ds_read_b32 v3, v3
	s_waitcnt lgkmcnt(1)
	v_sub_u32_e32 v4, s4, v4
	v_lshlrev_b32_e32 v4, 8, v4
	v_or_b32_e32 v5, v4, v0
	s_waitcnt lgkmcnt(0)
	v_cmp_lt_i32_e64 s[4:5], v5, v3
	v_mov_b32_e32 v3, 0
	v_mov_b32_e32 v12, 0
	s_and_saveexec_b64 s[16:17], s[4:5]
	s_cbranch_execz .LBB0_1052
	v_lshlrev_b32_e32 v2, 14, v2
	v_add_u32_e32 v2, v4, v2
	v_or_b32_e32 v2, v2, v0
	v_mov_b32_e32 v3, 0
	v_lshl_add_u64 v[2:3], v[2:3], 2, s[12:13]
	global_load_dword v12, v[2:3], off
.LBB0_1052:
	s_or_b64 exec, exec, s[16:17]
	s_mov_b64 s[78:79], exec
.LBB0_1053:
	s_or_b64 exec, exec, s[14:15]
	s_add_i32 s20, s20, s3
	s_cmp_lt_i32 s20, s25
	s_cselect_b64 s[4:5], -1, 0
	s_and_b64 s[4:5], s[4:5], vcc
	s_and_saveexec_b64 s[14:15], s[4:5]
	s_cbranch_execz .LBB0_1057
	s_mul_hi_i32 s4, s20, 0x2aaaaaab
	s_lshr_b32 s5, s4, 31
	s_add_i32 s4, s4, s5
	s_lshl_b32 s5, s4, 2
	s_add_i32 s5, s5, 0
	s_add_i32 s5, s5, 0x24280
	s_waitcnt vmcnt(7)
	v_mov_b32_e32 v2, s5
	ds_read_b32 v2, v2
	s_waitcnt lgkmcnt(0)
	v_lshlrev_b32_e32 v3, 2, v2
	v_add_u32_e32 v3, 0, v3
	v_add_u32_e32 v4, 0x24140, v3
	ds_read_b32 v4, v4
	v_add_u32_e32 v3, 0x24040, v3
	ds_read_b32 v3, v3
	s_waitcnt lgkmcnt(1)
	v_sub_u32_e32 v4, s4, v4
	v_lshlrev_b32_e32 v4, 8, v4
	v_or_b32_e32 v5, v4, v0
	s_waitcnt lgkmcnt(0)
	v_cmp_lt_i32_e64 s[4:5], v5, v3
	v_mov_b32_e32 v3, 0
	v_mov_b32_e32 v13, 0
	s_and_saveexec_b64 s[16:17], s[4:5]
	s_cbranch_execz .LBB0_1056
	v_lshlrev_b32_e32 v2, 14, v2
	v_add_u32_e32 v2, v4, v2
	v_or_b32_e32 v2, v2, v0
	v_mov_b32_e32 v3, 0
	v_lshl_add_u64 v[2:3], v[2:3], 2, s[12:13]
	global_load_dword v13, v[2:3], off
.LBB0_1056:
	s_or_b64 exec, exec, s[16:17]
	s_mov_b64 s[80:81], exec
.LBB0_1057:
	s_or_b64 exec, exec, s[14:15]
	s_add_i32 s20, s20, s3
	s_cmp_lt_i32 s20, s25
	s_cselect_b64 s[4:5], -1, 0
	s_and_b64 s[14:15], s[4:5], vcc
	s_and_saveexec_b64 s[4:5], s[14:15]
	s_cbranch_execz .LBB0_1061
	s_mul_hi_i32 s14, s20, 0x2aaaaaab
	s_lshr_b32 s15, s14, 31
	s_add_i32 s14, s14, s15
	s_lshl_b32 s15, s14, 2
	s_add_i32 s15, s15, 0
	s_add_i32 s15, s15, 0x24280
	s_waitcnt vmcnt(7)
	v_mov_b32_e32 v2, s15
	ds_read_b32 v2, v2
	s_waitcnt lgkmcnt(0)
	v_lshlrev_b32_e32 v3, 2, v2
	v_add_u32_e32 v3, 0, v3
	v_add_u32_e32 v4, 0x24140, v3
	ds_read_b32 v4, v4
	v_add_u32_e32 v3, 0x24040, v3
	ds_read_b32 v3, v3
	s_waitcnt lgkmcnt(1)
	v_sub_u32_e32 v4, s14, v4
	v_lshlrev_b32_e32 v4, 8, v4
	v_or_b32_e32 v5, v4, v0
	s_waitcnt lgkmcnt(0)
	v_cmp_lt_i32_e32 vcc, v5, v3
	v_mov_b32_e32 v3, 0
	v_mov_b32_e32 v14, 0
	s_and_saveexec_b64 s[14:15], vcc
	s_cbranch_execz .LBB0_1060
	v_lshlrev_b32_e32 v2, 14, v2
	v_add_u32_e32 v2, v4, v2
	v_or_b32_e32 v2, v2, v0
	v_mov_b32_e32 v3, 0
	v_lshl_add_u64 v[2:3], v[2:3], 2, s[12:13]
	global_load_dword v14, v[2:3], off
.LBB0_1060:
	s_or_b64 exec, exec, s[14:15]
	s_mov_b64 s[82:83], exec
.LBB0_1061:
	s_or_b64 exec, exec, s[4:5]
	s_mov_b64 s[84:85], exec
	s_waitcnt vmcnt(0)
	s_mov_b64 exec, s[74:75]
	ds_write_b32 v1, v10
	s_mov_b64 exec, s[76:77]
	ds_write_b32 v1, v11 offset:1024
	s_mov_b64 exec, s[78:79]
	ds_write_b32 v1, v12 offset:2048
	s_mov_b64 exec, s[80:81]
	ds_write_b32 v1, v13 offset:3072
	s_mov_b64 exec, s[82:83]
	ds_write_b32 v1, v14 offset:4096
	s_mov_b64 exec, s[84:85]
	v_readfirstlane_b32 s4, v0
	s_and_b64 vcc, exec, s[8:9]
	s_waitcnt lgkmcnt(0)
	s_barrier
	s_cbranch_vccz .LBB0_1086
	v_lshlrev_b32_e32 v1, 4, v0
	s_waitcnt vmcnt(7)
	v_and_b32_e32 v2, 32, v0
	v_bfe_u32 v4, v0, 3, 25
	v_bfe_u32 v3, v0, 2, 4
	v_bitop3_b32 v1, v1, v2, 48 bitop3:0x6c
	v_lshrrev_b32_e32 v2, 3, v0
	v_or_b32_e32 v4, 64, v4
	s_movk_i32 s8, 0x70
	s_add_u32 s12, s6, 0x2780a000
	v_and_or_b32 v206, v2, 48, v3
	v_and_or_b32 v207, v4, s8, v3
	v_lshrrev_b32_e32 v3, 5, v0
	s_waitcnt vmcnt(6)
	v_lshrrev_b32_e32 v6, 1, v0
	s_addc_u32 s13, s7, 0
	v_and_b32_e32 v3, 4, v3
	v_bfe_u32 v5, v0, 2, 2
	v_and_b32_e32 v6, 24, v6
	s_add_u32 s46, s6, 0x380a000
	v_or3_b32 v3, v3, v5, v6
	s_movk_i32 s8, 0x60
	s_addc_u32 s47, s7, 0
	v_and_or_b32 v4, v4, s8, v3
	s_lshr_b32 s8, s19, 31
	s_add_i32 s69, s19, s8
	s_mul_i32 s8, s69, -6
	s_add_i32 s30, s8, s44
	s_lshl_b32 s8, s69, 2
	s_add_i32 s8, s8, 0
	v_and_or_b32 v1, v0, 64, v1
	s_lshr_b32 s20, s4, 6
	v_and_or_b32 v2, v2, 32, v3
	s_add_i32 s8, s8, 0x24280
	s_ashr_i32 s31, s30, 31
	s_lshr_b32 s5, s4, 8
	s_lshl_b32 s52, s20, 10
	v_lshl_or_b32 v196, v2, 11, v1
	v_mov_b32_e32 v2, s8
	s_lshl_b64 s[8:9], s[30:31], 19
	s_add_u32 s8, s46, s8
	s_addc_u32 s9, s47, s9
	v_lshlrev_b32_e32 v3, 2, v206
	v_lshlrev_b32_e32 v5, 2, v207
	s_add_i32 s14, 0, 0x24800
	v_lshl_or_b32 v194, v4, 11, v1
	v_add_u32_e32 v4, s18, v3
	v_add_u32_e32 v7, s18, v5
	v_add_u32_e32 v3, s14, v3
	v_add_u32_e32 v5, s14, v5
	ds_read_b32 v2, v2
	ds_read_b32 v4, v4
	ds_read_b32 v9, v7
	ds_read_b32 v3, v3
	ds_read_b32 v5, v5
	s_waitcnt lgkmcnt(4)
	v_readfirstlane_b32 s14, v2
	s_mul_hi_i32 s15, s14, 0x300000
	s_mul_i32 s14, s14, 0x300000
	s_add_u32 s8, s8, s14
	v_lshlrev_b32_e32 v7, 2, v2
	s_addc_u32 s9, s9, s15
	s_add_i32 s31, s52, 0
	v_add_u32_e32 v7, 0, v7
	s_add_i32 s53, s31, 0x10000
	s_add_i32 s54, s31, 0x12000
	v_add_u32_e32 v8, 0x24140, v7
	v_add_u32_e32 v7, 0x24040, v7
	s_mov_b32 m0, s53
	s_add_u32 s14, s8, 0x40000
	ds_read_b32 v8, v8
	ds_read_b32 v7, v7
	global_load_lds_dwordx4 v196, s[8:9]
	s_mov_b32 m0, s54
	s_addc_u32 s15, s9, 0
	s_add_i32 s55, s31, 0x14000
	global_load_lds_dwordx4 v194, s[8:9]
	s_mov_b32 m0, s55
	s_add_i32 s56, s31, 0x16000
	global_load_lds_dwordx4 v196, s[14:15]
	s_mov_b32 m0, s56
	s_waitcnt lgkmcnt(0)
	v_lshl_or_b32 v198, v4, 11, v1
	global_load_lds_dwordx4 v194, s[14:15]
	s_mov_b32 m0, s31
	s_add_i32 s57, s31, 0x2000
	v_lshl_or_b32 v200, v9, 11, v1
	global_load_lds_dwordx4 v198, s[12:13]
	s_mov_b32 m0, s57
	s_add_i32 s58, s31, 0x4000
	v_lshl_or_b32 v208, v3, 11, v1
	global_load_lds_dwordx4 v200, s[12:13]
	s_mov_b32 m0, s58
	s_add_i32 s59, s31, 0x6000
	v_lshl_or_b32 v209, v5, 11, v1
	global_load_lds_dwordx4 v208, s[12:13]
	s_mov_b32 m0, s59
	v_mov_b32_e32 v199, 0
	global_load_lds_dwordx4 v209, s[12:13]
	v_mov_b32_e32 v197, v199
	v_mov_b32_e32 v195, v199
	s_cmp_eq_u32 s5, 1
	s_mov_b32 s60, 0
	v_lshl_add_u64 v[4:5], s[8:9], 0, v[196:197]
	v_lshl_add_u64 v[2:3], s[8:9], 0, v[194:195]
	s_cselect_b64 s[14:15], -1, 0
	s_cmp_lg_u32 s5, 1
	v_mov_b32_e32 v201, v199
	s_cbranch_scc1 .LBB0_1064
	s_barrier

	.amdhsa_kernel _Z4mega4Args
		.amdhsa_group_segment_fixed_size 0
		.amdhsa_private_segment_fixed_size 0
		.amdhsa_kernarg_size 472
		.amdhsa_user_sgpr_count 2
		.amdhsa_user_sgpr_dispatch_ptr 0
		.amdhsa_user_sgpr_queue_ptr 0
		.amdhsa_user_sgpr_kernarg_segment_ptr 1
		.amdhsa_user_sgpr_dispatch_id 0
		.amdhsa_user_sgpr_kernarg_preload_length 0
		.amdhsa_user_sgpr_kernarg_preload_offset 0
		.amdhsa_user_sgpr_private_segment_size 0
		.amdhsa_uses_dynamic_stack 0
		.amdhsa_enable_private_segment 0
		.amdhsa_system_sgpr_workgroup_id_x 1
		.amdhsa_system_sgpr_workgroup_id_y 0
		.amdhsa_system_sgpr_workgroup_id_z 0
		.amdhsa_system_sgpr_workgroup_info 0
		.amdhsa_system_vgpr_workitem_id 0
		.amdhsa_next_free_vgpr 254
		.amdhsa_next_free_sgpr 98
		.amdhsa_accum_offset 256
		.amdhsa_reserve_vcc 1
		.amdhsa_float_round_mode_32 0
		.amdhsa_float_round_mode_16_64 0
		.amdhsa_float_denorm_mode_32 3
		.amdhsa_float_denorm_mode_16_64 3
		.amdhsa_dx10_clamp 1
		.amdhsa_ieee_mode 1
		.amdhsa_fp16_overflow 0
		.amdhsa_tg_split 0
		.amdhsa_exception_fp_ieee_invalid_op 0
		.amdhsa_exception_fp_denorm_src 0
		.amdhsa_exception_fp_ieee_div_zero 0
		.amdhsa_exception_fp_ieee_overflow 0
		.amdhsa_exception_fp_ieee_underflow 0
		.amdhsa_exception_fp_ieee_inexact 0
		.amdhsa_exception_int_div_zero 0
	.end_amdhsa_kernel

amdhsa.kernels:
  - .agpr_count:     0
    .args:
      - .offset:         0
        .size:           216
        .value_kind:     by_value
      - .offset:         216
        .size:           4
        .value_kind:     hidden_block_count_x
      - .offset:         220
        .size:           4
        .value_kind:     hidden_block_count_y
      - .offset:         224
        .size:           4
        .value_kind:     hidden_block_count_z
      - .offset:         228
        .size:           2
        .value_kind:     hidden_group_size_x
      - .offset:         230
        .size:           2
        .value_kind:     hidden_group_size_y
      - .offset:         232
        .size:           2
        .value_kind:     hidden_group_size_z
      - .offset:         234
        .size:           2
        .value_kind:     hidden_remainder_x
      - .offset:         236
        .size:           2
        .value_kind:     hidden_remainder_y
      - .offset:         238
        .size:           2
        .value_kind:     hidden_remainder_z
      - .offset:         256
        .size:           8
        .value_kind:     hidden_global_offset_x
      - .offset:         264
        .size:           8
        .value_kind:     hidden_global_offset_y
      - .offset:         272
        .size:           8
        .value_kind:     hidden_global_offset_z
      - .offset:         280
        .size:           2
        .value_kind:     hidden_grid_dims
      - .offset:         336
        .size:           4
        .value_kind:     hidden_dynamic_lds_size
    .group_segment_fixed_size: 0
    .kernarg_segment_align: 8
    .kernarg_segment_size: 472
    .language:       OpenCL C
    .language_version:
      - 2
      - 0
    .max_flat_workgroup_size: 512
    .name:           _Z4mega4Args
    .private_segment_fixed_size: 0
    .sgpr_count:     104
    .sgpr_spill_count: 2
    .symbol:         _Z4mega4Args.kd
    .uniform_work_group_size: 1
    .uses_dynamic_stack: false
    .vgpr_count:     254
    .vgpr_spill_count: 0
    .wavefront_size: 64
